# baseline (speedup 1.0000x reference)
.Lq_noprio:
	s_waitcnt vmcnt(12)
	v_cvt_pk_f16_f32 v164, v36, v40
	v_cvt_pk_f16_f32 v180, v68, v72
	v_pk_add_f16 v164, v164, -0.5 op_sel_hi:[1,0]
	v_pk_add_f16 v180, v180, -0.5 op_sel_hi:[1,0]
	v_pk_mul_f16 v196, v180, v180
	v_pk_mul_f16 v212, v164, v180
	v_pk_fma_f16 v196, v164, v164, v196
	v_cvt_pk_f16_f32 v168, v37, v41
	v_cvt_pk_f16_f32 v184, v69, v73
	v_pk_add_f16 v168, v168, -0.5 op_sel_hi:[1,0]
	v_pk_add_f16 v184, v184, -0.5 op_sel_hi:[1,0]
	v_pk_mul_f16 v200, v184, v184
	v_pk_mul_f16 v216, v168, v184
	v_pk_fma_f16 v200, v168, v168, v200
	v_cvt_pk_f16_f32 v172, v38, v42
	v_cvt_pk_f16_f32 v188, v70, v74
	v_pk_add_f16 v172, v172, -0.5 op_sel_hi:[1,0]
	v_pk_add_f16 v188, v188, -0.5 op_sel_hi:[1,0]
	v_pk_mul_f16 v204, v188, v188
	v_pk_mul_f16 v220, v172, v188
	v_pk_fma_f16 v204, v172, v172, v204
	v_cvt_pk_f16_f32 v176, v39, v43
	v_cvt_pk_f16_f32 v192, v71, v75
	v_pk_add_f16 v176, v176, -0.5 op_sel_hi:[1,0]
	v_pk_add_f16 v192, v192, -0.5 op_sel_hi:[1,0]
	v_pk_mul_f16 v208, v192, v192
	v_pk_mul_f16 v224, v176, v192
	v_pk_fma_f16 v208, v176, v176, v208
	s_waitcnt vmcnt(8)
	v_cvt_pk_f16_f32 v165, v44, v48
	v_cvt_pk_f16_f32 v181, v76, v80
	v_pk_add_f16 v165, v165, -0.5 op_sel_hi:[1,0]
	v_pk_add_f16 v181, v181, -0.5 op_sel_hi:[1,0]
	v_pk_mul_f16 v197, v181, v181
	v_pk_mul_f16 v213, v165, v181
	v_pk_fma_f16 v197, v165, v165, v197
	v_cvt_pk_f16_f32 v169, v45, v49
	v_cvt_pk_f16_f32 v185, v77, v81
	v_pk_add_f16 v169, v169, -0.5 op_sel_hi:[1,0]
	v_pk_add_f16 v185, v185, -0.5 op_sel_hi:[1,0]
	v_pk_mul_f16 v201, v185, v185
	v_pk_mul_f16 v217, v169, v185
	v_pk_fma_f16 v201, v169, v169, v201
	v_cvt_pk_f16_f32 v173, v46, v50
	v_cvt_pk_f16_f32 v189, v78, v82
	v_pk_add_f16 v173, v173, -0.5 op_sel_hi:[1,0]
	v_pk_add_f16 v189, v189, -0.5 op_sel_hi:[1,0]
	v_pk_mul_f16 v205, v189, v189
	v_pk_mul_f16 v221, v173, v189
	v_pk_fma_f16 v205, v173, v173, v205
	v_cvt_pk_f16_f32 v177, v47, v51
	v_cvt_pk_f16_f32 v193, v79, v83
	v_pk_add_f16 v177, v177, -0.5 op_sel_hi:[1,0]
	v_pk_add_f16 v193, v193, -0.5 op_sel_hi:[1,0]
	v_pk_mul_f16 v209, v193, v193
	v_pk_mul_f16 v225, v177, v193
	v_pk_fma_f16 v209, v177, v177, v209
	global_load_dwordx4 v[100:103], v240, s[18:19] offset:0 sc1 nt
	global_load_dwordx4 v[104:107], v240, s[18:19] offset:2048 sc1 nt
	global_load_dwordx4 v[132:135], v240, s[20:21] offset:0 sc1 nt
	global_load_dwordx4 v[136:139], v240, s[20:21] offset:2048 sc1 nt
	global_load_dwordx4 v[108:111], v241, s[18:19] offset:0 sc1 nt
	global_load_dwordx4 v[112:115], v241, s[18:19] offset:2048 sc1 nt
	global_load_dwordx4 v[140:143], v241, s[20:21] offset:0 sc1 nt
	global_load_dwordx4 v[144:147], v241, s[20:21] offset:2048 sc1 nt
	global_load_dwordx4 v[116:119], v242, s[18:19] offset:0 sc1 nt
	global_load_dwordx4 v[120:123], v242, s[18:19] offset:2048 sc1 nt
	global_load_dwordx4 v[148:151], v242, s[20:21] offset:0 sc1 nt
	global_load_dwordx4 v[152:155], v242, s[20:21] offset:2048 sc1 nt
	global_load_dwordx4 v[124:127], v243, s[18:19] offset:0 sc1 nt
	global_load_dwordx4 v[128:131], v243, s[18:19] offset:2048 sc1 nt
	global_load_dwordx4 v[156:159], v243, s[20:21] offset:0 sc1 nt
	global_load_dwordx4 v[160:163], v243, s[20:21] offset:2048 sc1 nt
	s_waitcnt vmcnt(20)
	v_cvt_pk_f16_f32 v166, v52, v56
	v_cvt_pk_f16_f32 v182, v84, v88
	v_pk_add_f16 v166, v166, -0.5 op_sel_hi:[1,0]
	v_pk_add_f16 v182, v182, -0.5 op_sel_hi:[1,0]
	v_pk_mul_f16 v198, v182, v182
	v_pk_mul_f16 v214, v166, v182
	v_pk_fma_f16 v198, v166, v166, v198
	v_cvt_pk_f16_f32 v170, v53, v57
	v_cvt_pk_f16_f32 v186, v85, v89
	v_pk_add_f16 v170, v170, -0.5 op_sel_hi:[1,0]
	v_pk_add_f16 v186, v186, -0.5 op_sel_hi:[1,0]
	v_pk_mul_f16 v202, v186, v186
	v_pk_mul_f16 v218, v170, v186
	v_pk_fma_f16 v202, v170, v170, v202
	v_cvt_pk_f16_f32 v174, v54, v58
	v_cvt_pk_f16_f32 v190, v86, v90
	v_pk_add_f16 v174, v174, -0.5 op_sel_hi:[1,0]
	v_pk_add_f16 v190, v190, -0.5 op_sel_hi:[1,0]
	v_pk_mul_f16 v206, v190, v190
	v_pk_mul_f16 v222, v174, v190
	v_pk_fma_f16 v206, v174, v174, v206
	v_cvt_pk_f16_f32 v178, v55, v59
	v_cvt_pk_f16_f32 v194, v87, v91
	v_pk_add_f16 v178, v178, -0.5 op_sel_hi:[1,0]
	v_pk_add_f16 v194, v194, -0.5 op_sel_hi:[1,0]
	v_pk_mul_f16 v210, v194, v194
	v_pk_mul_f16 v226, v178, v194
	v_pk_fma_f16 v210, v178, v178, v210
	s_waitcnt vmcnt(16)
	v_cvt_pk_f16_f32 v167, v60, v64
	v_cvt_pk_f16_f32 v183, v92, v96
	v_pk_add_f16 v167, v167, -0.5 op_sel_hi:[1,0]
	v_pk_add_f16 v183, v183, -0.5 op_sel_hi:[1,0]
	v_pk_mul_f16 v199, v183, v183
	v_pk_mul_f16 v215, v167, v183
	v_pk_fma_f16 v199, v167, v167, v199
	v_cvt_pk_f16_f32 v171, v61, v65
	v_cvt_pk_f16_f32 v187, v93, v97
	v_pk_add_f16 v171, v171, -0.5 op_sel_hi:[1,0]
	v_pk_add_f16 v187, v187, -0.5 op_sel_hi:[1,0]
	v_pk_mul_f16 v203, v187, v187
	v_pk_mul_f16 v219, v171, v187
	v_pk_fma_f16 v203, v171, v171, v203
	v_cvt_pk_f16_f32 v175, v62, v66
	v_cvt_pk_f16_f32 v191, v94, v98
	v_pk_add_f16 v175, v175, -0.5 op_sel_hi:[1,0]
	v_pk_add_f16 v191, v191, -0.5 op_sel_hi:[1,0]
	v_pk_mul_f16 v207, v191, v191
	v_pk_mul_f16 v223, v175, v191
	v_pk_fma_f16 v207, v175, v175, v207
	v_cvt_pk_f16_f32 v179, v63, v67
	v_cvt_pk_f16_f32 v195, v95, v99
	v_pk_add_f16 v179, v179, -0.5 op_sel_hi:[1,0]
	v_pk_add_f16 v195, v195, -0.5 op_sel_hi:[1,0]
	v_pk_mul_f16 v211, v195, v195
	v_pk_mul_f16 v227, v179, v195
	v_pk_fma_f16 v211, v179, v179, v211
	v_mfma_f32_16x16x32_f16 v[68:71], v[164:167], v[24:27], 0
	v_mfma_f32_16x16x32_f16 v[72:75], v[168:171], v[24:27], 0
	v_mfma_f32_16x16x32_f16 v[76:79], v[172:175], v[24:27], 0
	v_mfma_f32_16x16x32_f16 v[80:83], v[176:179], v[24:27], 0
	v_mfma_f32_16x16x32_f16 v[84:87], v[180:183], v[24:27], 0
	v_mfma_f32_16x16x32_f16 v[88:91], v[184:187], v[24:27], 0
	v_mfma_f32_16x16x32_f16 v[92:95], v[188:191], v[24:27], 0
	v_mfma_f32_16x16x32_f16 v[96:99], v[192:195], v[24:27], 0
	s_nop 1
	v_cvt_pk_f16_f32 v36, v68, v72
	s_nop 0
	v_cvt_pk_f16_f32 v37, v76, v80
	v_cvt_pk_f16_f32 v38, v69, v73
	v_cvt_pk_f16_f32 v39, v77, v81
	v_cvt_pk_f16_f32 v40, v70, v74
	v_cvt_pk_f16_f32 v41, v78, v82
	v_cvt_pk_f16_f32 v42, v71, v75
	v_cvt_pk_f16_f32 v43, v79, v83
	v_mfma_f32_16x16x32_f16 v[68:71], v[196:199], v[24:27], 0
	v_mfma_f32_16x16x32_f16 v[72:75], v[200:203], v[24:27], 0
	v_mfma_f32_16x16x32_f16 v[76:79], v[204:207], v[24:27], 0
	v_mfma_f32_16x16x32_f16 v[80:83], v[208:211], v[24:27], 0
	v_cvt_pk_f16_f32 v44, v84, v88
	v_cvt_pk_f16_f32 v45, v92, v96
	v_cvt_pk_f16_f32 v46, v85, v89
	v_cvt_pk_f16_f32 v47, v93, v97
	v_cvt_pk_f16_f32 v48, v86, v90
	v_cvt_pk_f16_f32 v49, v94, v98
	v_cvt_pk_f16_f32 v50, v87, v91
	v_cvt_pk_f16_f32 v51, v95, v99
	v_mfma_f32_16x16x32_f16 v[84:87], v[212:215], v[24:27], 0
	v_mfma_f32_16x16x32_f16 v[88:91], v[216:219], v[24:27], 0
	v_mfma_f32_16x16x32_f16 v[92:95], v[220:223], v[24:27], 0
	v_mfma_f32_16x16x32_f16 v[96:99], v[224:227], v[24:27], 0
	v_cvt_pk_f16_f32 v52, v68, v72
	v_cvt_pk_f16_f32 v53, v76, v80
	v_cvt_pk_f16_f32 v54, v69, v73
	v_cvt_pk_f16_f32 v55, v77, v81
	v_cvt_pk_f16_f32 v56, v70, v74
	v_cvt_pk_f16_f32 v57, v78, v82
	v_cvt_pk_f16_f32 v58, v71, v75
	v_cvt_pk_f16_f32 v59, v79, v83
	v_cvt_pk_f16_f32 v60, v84, v88
	v_cvt_pk_f16_f32 v61, v92, v96
	v_cvt_pk_f16_f32 v62, v85, v89
	v_cvt_pk_f16_f32 v63, v93, v97
	v_cvt_pk_f16_f32 v64, v86, v90
	v_cvt_pk_f16_f32 v65, v94, v98
	v_cvt_pk_f16_f32 v66, v87, v91
	v_cvt_pk_f16_f32 v67, v95, v99
	s_mov_b64 exec, s[38:39]
	ds_write_b128 v4, v[40:43] offset:0
	ds_write_b128 v4, v[48:51] offset:512
	ds_write_b128 v4, v[56:59] offset:1024
	ds_write_b128 v4, v[64:67] offset:1536
	s_mov_b64 exec, -1
	v_mfma_f32_16x16x32_f16 v[68:71], v[24:27], v[36:39], 0
	v_mfma_f32_16x16x32_f16 v[72:75], v[24:27], v[44:47], 0
	v_mfma_f32_16x16x32_f16 v[76:79], v[24:27], v[52:55], v[0:3]
	v_mfma_f32_16x16x32_f16 v[80:83], v[24:27], v[60:63], 0
	v_mfma_f32_16x16x32_f16 v[84:87], v[28:31], v[36:39], 0
	v_mfma_f32_16x16x32_f16 v[88:91], v[28:31], v[44:47], 0
	v_mfma_f32_16x16x32_f16 v[92:95], v[28:31], v[52:55], v[0:3]
	v_mfma_f32_16x16x32_f16 v[96:99], v[28:31], v[60:63], 0
	v_mfma_f32_16x16x32_f16 v[84:87], v[32:35], v[40:43], v[84:87]
	v_mfma_f32_16x16x32_f16 v[88:91], v[32:35], v[48:51], v[88:91]
	v_mfma_f32_16x16x32_f16 v[92:95], v[32:35], v[56:59], v[92:95]
	v_mfma_f32_16x16x32_f16 v[96:99], v[32:35], v[64:67], v[96:99]
	s_waitcnt lgkmcnt(0)
	ds_write_b32 v6, v6 offset:0
	ds_read_b32 v9, v7 offset:0
	v_mul_f32_e32 v244, v68, v72
	v_mul_f32_e32 v250, v69, v73
	v_mul_f32_e64 v245, -v72, v72
	v_mul_f32_e64 v251, -v73, v73
	v_add_f32_e32 v246, v68, v72
	v_add_f32_e32 v252, v69, v73
	v_fma_f32 v245, -v68, v68, v245
	v_fma_f32 v251, -v69, v69, v251
	v_fma_f32 v247, v10, v246, v11
	v_fma_f32 v253, v10, v252, v11
	v_fma_f32 v246, v13, v80, v14
	v_fma_f32 v252, v13, v81, v14
	v_fma_f32 v248, v12, v76, v245
	v_fma_f32 v254, v12, v77, v251
	v_fma_f32 v249, 2.0, v244, v247
	v_fma_f32 v255, 2.0, v250, v253
	v_sub_f32_e32 v247, v247, v245
	v_sub_f32_e32 v253, v253, v251
	v_fma_f32 v246, -2.0, v244, v246
	v_fma_f32 v252, -2.0, v250, v252
	v_mul_f32_e32 v247, v247, v248
	v_mul_f32_e32 v253, v253, v254
	v_rcp_f32_e32 v247, v247
	v_rcp_f32_e32 v253, v253
	v_mul_f32_e32 v249, v249, v246
	v_mul_f32_e32 v255, v255, v252
	v_fma_f32 v19, v249, v247, v19
	v_fma_f32 v19, v255, v253, v19
	v_mul_f32_e32 v244, v70, v74
	v_mul_f32_e32 v250, v71, v75
	v_mul_f32_e64 v245, -v74, v74
	v_mul_f32_e64 v251, -v75, v75
	v_add_f32_e32 v246, v70, v74
	v_add_f32_e32 v252, v71, v75
	v_fma_f32 v245, -v70, v70, v245
	v_fma_f32 v251, -v71, v71, v251
	v_fma_f32 v247, v10, v246, v11
	v_fma_f32 v253, v10, v252, v11
	v_fma_f32 v246, v13, v82, v14
	v_fma_f32 v252, v13, v83, v14
	v_fma_f32 v248, v12, v78, v245
	v_fma_f32 v254, v12, v79, v251
	v_fma_f32 v249, 2.0, v244, v247
	v_fma_f32 v255, 2.0, v250, v253
	v_sub_f32_e32 v247, v247, v245
	v_sub_f32_e32 v253, v253, v251
	v_fma_f32 v246, -2.0, v244, v246
	v_fma_f32 v252, -2.0, v250, v252
	v_mul_f32_e32 v247, v247, v248
	v_mul_f32_e32 v253, v253, v254
	v_rcp_f32_e32 v247, v247
	v_rcp_f32_e32 v253, v253
	v_mul_f32_e32 v249, v249, v246
	v_mul_f32_e32 v255, v255, v252
	v_fma_f32 v20, v249, v247, v20
	v_fma_f32 v20, v255, v253, v20
	v_mfma_f32_16x16x32_f16 v[68:71], v[24:27], v[40:43], 0
	v_mfma_f32_16x16x32_f16 v[72:75], v[24:27], v[48:51], 0
	v_mfma_f32_16x16x32_f16 v[76:79], v[24:27], v[56:59], v[0:3]
	v_mfma_f32_16x16x32_f16 v[80:83], v[24:27], v[64:67], 0
	s_barrier
	ds_read_b32 v9, v7 offset:0
	s_waitcnt lgkmcnt(0)
	v_cmp_ne_u32_e32 vcc, 0, v9
	s_cbranch_vccnz .Lq_go_0
